# baseline (speedup 1.0000x reference)
.LBB0_43:
	s_or_b64 exec, exec, s[6:7]
	s_cmp_lg_u32 s2, 0
	s_cbranch_scc1 .LBB0_46
	s_load_dwordx4 s[0:3], s[0:1], 0x30
	v_lshrrev_b32_e32 v1, 4, v0
	v_and_b32_e32 v1, 28, v1
	v_lshl_or_b32 v6, v34, 8, v1
	v_mov_b32_e32 v7, 0
	s_waitcnt lgkmcnt(0)
	v_lshl_add_u64 v[2:3], s[0:1], 0, v[6:7]
	v_lshlrev_b32_e32 v6, 1, v0
	v_lshl_add_u64 v[0:1], s[2:3], 0, v[6:7]
	s_mov_b64 s[2:3], 0x1000
	global_load_dword v8, v[2:3], off
	global_load_dword v9, v[2:3], off offset:32
	global_load_dword v10, v[2:3], off offset:64
	global_load_dword v11, v[2:3], off offset:96
	global_load_dword v12, v[2:3], off offset:128
	global_load_dword v13, v[2:3], off offset:160
	global_load_dword v14, v[2:3], off offset:192
	global_load_dword v15, v[2:3], off offset:224
	v_lshl_add_u64 v[4:5], v[0:1], 0, s[2:3]
	s_waitcnt vmcnt(0)
	v_cvt_f16_f32_e32 v8, v8
	v_cvt_f16_f32_e32 v9, v9
	v_cvt_f16_f32_e32 v10, v10
	v_cvt_f16_f32_e32 v11, v11
	v_cvt_f16_f32_e32 v12, v12
	v_cvt_f16_f32_e32 v13, v13
	v_cvt_f16_f32_e32 v14, v14
	v_cvt_f16_f32_e32 v15, v15
	global_store_short v[0:1], v8, off
	global_store_short v[0:1], v9, off offset:1024
	global_store_short v[0:1], v10, off offset:2048
	global_store_short v[0:1], v11, off offset:3072
	global_store_short v[4:5], v12, off
	global_store_short v[4:5], v13, off offset:1024
	global_store_short v[4:5], v14, off offset:2048
	global_store_short v[4:5], v15, off offset:3072
